# attention unit: the eight Q-row loads are issued at the top of the unit together with the log-forget loads (addresses from the unit coordinates) instead of after the scan and its barriers
# baseline (speedup 1.0000x reference)
.LBB0_400:
	s_mov_b64 s[8:9], -1
	s_and_b64 vcc, exec, s[6:7]
	s_cbranch_vccz .LBB0_393
	s_mov_b64 s[6:7], s[0:1]
	s_load_dwordx2 s[14:15], s[6:7], 0xd0
	s_ashr_i32 s18, s4, 3
	v_mbcnt_lo_u32_b32 v0, -1, 0
	v_mbcnt_hi_u32_b32 v0, -1, v0
	s_ashr_i32 s19, s18, 31
	v_add_u32_e32 v8, s67, v0
	s_lshl_b64 s[16:17], s[18:19], 11
	v_lshlrev_b32_e32 v2, 2, v8
	v_ashrrev_i32_e32 v3, 31, v2
	v_lshl_add_u64 v[4:5], s[16:17], 0, v[2:3]
	s_and_b32 s23, s4, 7
	v_lshlrev_b64 v[4:5], 5, v[4:5]
	s_waitcnt lgkmcnt(0)
	v_lshl_add_u64 v[4:5], s[14:15], 0, v[4:5]
	s_lshl_b32 s52, s23, 2
	v_lshl_add_u64 v[4:5], v[4:5], 0, s[52:53]
	s_mov_b64 s[4:5], 0x100000
	v_lshl_add_u64 v[6:7], v[4:5], 0, s[4:5]
	s_mov_b32 s4, 0x100000
	v_add_co_u32_e32 v4, vcc, s4, v4
	v_and_b32_e32 v9, 64, v234
	s_nop 0
	v_addc_co_u32_e32 v5, vcc, 0, v5, vcc
	global_load_dword v4, v[4:5], off
	s_nop 0
	global_load_dword v0, v[6:7], off offset:32
	global_load_dword v3, v[6:7], off offset:64
	s_nop 0
	global_load_dword v7, v[6:7], off offset:96
	s_lshl_b32 s100, s18, 2
	s_add_u32 s100, s100, s12
	s_addc_u32 s101, s13, 0
	s_add_u32 s100, s100, s14
	s_addc_u32 s101, s101, s15
	v_mov_b32_e32 v241, 0x20000
	global_load_dword v240, v241, s[100:101] sc1
	v_add_u32_e32 v5, -1, v234
	s_lshl_b32 s100, s25, 9
	s_add_i32 s100, s100, s67
	v_and_b32_e32 v56, 31, v234
	v_or_b32_e32 v56, s100, v56
	v_ashrrev_i32_e32 v57, 31, v56
	v_lshl_add_u64 v[56:57], s[16:17], 0, v[56:57]
	v_lshlrev_b64 v[56:57], 10, v[56:57]
	v_lshl_add_u64 v[56:57], s[14:15], 0, v[56:57]
	s_lshl_b32 s100, s23, 7
	s_mov_b32 s101, 0
	v_lshl_add_u64 v[56:57], v[56:57], 0, s[100:101]
	v_lshrrev_b32_e32 v58, 5, v234
	v_lshlrev_b32_e32 v58, 4, v58
	v_mov_b32_e32 v59, 0
	v_lshl_add_u64 v[56:57], v[56:57], 0, v[58:59]
	s_mov_b32 s100, 0x5c00000
	v_lshl_add_u64 v[58:59], v[56:57], 0, s[100:101]
	s_mov_b32 s100, 0x5c08000
	v_lshl_add_u64 v[56:57], v[56:57], 0, s[100:101]
	global_load_dwordx4 v[60:63], v[58:59], off
	global_load_dwordx4 v[64:67], v[56:57], off
	global_load_dwordx4 v[68:71], v[58:59], off offset:32
	global_load_dwordx4 v[72:75], v[56:57], off offset:32
	global_load_dwordx4 v[76:79], v[58:59], off offset:64
	global_load_dwordx4 v[80:83], v[56:57], off offset:64
	global_load_dwordx4 v[84:87], v[58:59], off offset:96
	global_load_dwordx4 v[88:91], v[56:57], off offset:96
	v_cmp_lt_i32_e32 vcc, v5, v9
	v_add_u32_e32 v10, -2, v234
	v_readfirstlane_b32 s5, v8
	v_cndmask_b32_e32 v5, v5, v234, vcc
	v_lshlrev_b32_e32 v11, 2, v5
	v_cmp_lt_i32_e32 vcc, v10, v9
	s_ashr_i32 s4, s5, 6
	s_waitcnt vmcnt(8)
	v_add_f32_e32 v5, v4, v0
	v_add_f32_e32 v6, v3, v5
	v_add_f32_e32 v7, v7, v6
	ds_bpermute_b32 v0, v11, v7
	v_cndmask_b32_e32 v3, v10, v234, vcc
	v_and_b32_e32 v10, 63, v8
	v_cmp_eq_u32_e32 vcc, 0, v10
	v_lshlrev_b32_e32 v3, 2, v3
	s_waitcnt lgkmcnt(0)
	v_add_f32_e32 v0, v7, v0
	v_cndmask_b32_e32 v0, v0, v7, vcc
	ds_bpermute_b32 v3, v3, v0
	v_add_u32_e32 v11, -4, v234
	v_cmp_lt_i32_e32 vcc, v11, v9
	s_waitcnt lgkmcnt(0)
	v_add_f32_e32 v3, v0, v3
	v_cndmask_b32_e32 v11, v11, v234, vcc
	v_cmp_gt_u32_e32 vcc, 2, v10
	v_lshlrev_b32_e32 v11, 2, v11
	s_nop 0
	v_cndmask_b32_e32 v0, v3, v0, vcc
	ds_bpermute_b32 v3, v11, v0
	v_add_u32_e32 v11, -8, v234
	v_cmp_lt_i32_e32 vcc, v11, v9
	s_waitcnt lgkmcnt(0)
	v_add_f32_e32 v3, v0, v3
	v_cndmask_b32_e32 v11, v11, v234, vcc
	v_cmp_gt_u32_e32 vcc, 4, v10
	v_lshlrev_b32_e32 v11, 2, v11
	s_nop 0
	v_cndmask_b32_e32 v0, v3, v0, vcc
	ds_bpermute_b32 v3, v11, v0
	v_add_u32_e32 v11, -16, v234
	v_cmp_lt_i32_e32 vcc, v11, v9
	s_waitcnt lgkmcnt(0)
	v_add_f32_e32 v3, v0, v3
	v_cndmask_b32_e32 v11, v11, v234, vcc
	v_cmp_gt_u32_e32 vcc, 8, v10
	v_lshlrev_b32_e32 v11, 2, v11
	s_nop 0
	v_cndmask_b32_e32 v0, v3, v0, vcc
	ds_bpermute_b32 v3, v11, v0
	v_subrev_u32_e32 v11, 32, v234
	v_cmp_lt_i32_e32 vcc, v11, v9
	s_waitcnt lgkmcnt(0)
	v_add_f32_e32 v3, v0, v3
	v_cndmask_b32_e32 v11, v11, v234, vcc
	v_cmp_gt_u32_e32 vcc, 16, v10
	v_lshlrev_b32_e32 v11, 2, v11
	s_nop 0
	v_cndmask_b32_e32 v0, v3, v0, vcc
	ds_bpermute_b32 v3, v11, v0
	v_cmp_eq_u32_e32 vcc, 63, v10
	s_waitcnt lgkmcnt(0)
	v_add_f32_e32 v11, v0, v3
	s_and_saveexec_b64 s[8:9], vcc
	s_lshl_b32 s10, s4, 2
	s_add_i32 s10, s10, 0
	v_mov_b32_e32 v3, s10
	ds_write_b32 v3, v11 offset:45056
	s_or_b64 exec, exec, s[8:9]
	s_load_dwordx4 s[8:11], s[6:7], 0x20
	s_cmp_lt_i32 s4, 1
	v_mov_b32_e32 v12, 0
	s_waitcnt lgkmcnt(0)
	s_barrier
	s_cbranch_scc1 .LBB0_406
	s_mov_b32 s6, s4
	v_readlane_b32 s7, v254, 60

.LBB0_406:
	s_lshl_b64 s[6:7], s[38:39], 2
	s_add_u32 s20, s8, s6
	s_addc_u32 s21, s9, s7
	s_add_u32 s8, s10, s6
	s_addc_u32 s9, s11, s7
	v_cmp_gt_u32_e64 s[6:7], 32, v10
	s_lshl_b32 s10, s25, 9
	s_and_b32 s24, s5, 0xffffffc0
	v_cndmask_b32_e64 v0, v11, v0, s[6:7]
	v_and_b32_e32 v3, 31, v8
	v_add_f32_e32 v0, v0, v12
	s_add_i32 s24, s24, s10
	v_sub_f32_e32 v0, v0, v7
	v_or_b32_e32 v172, s24, v3
	v_pk_add_f32 v[4:5], v[4:5], v[0:1] op_sel_hi:[1,0]
	v_pk_add_f32 v[6:7], v[6:7], v[0:1] op_sel_hi:[1,0]
	v_ashrrev_i32_e32 v173, 31, v172
	v_pk_mul_f32 v[6:7], v[6:7], s[66:67] op_sel_hi:[1,0]
	v_pk_mul_f32 v[4:5], v[4:5], s[66:67] op_sel_hi:[1,0]
	v_lshl_add_u32 v0, v2, 2, 0
	v_lshl_add_u64 v[174:175], s[16:17], 0, v[172:173]
	ds_write_b128 v0, v[4:7] offset:36864
	v_lshlrev_b64 v[4:5], 10, v[174:175]
	v_lshrrev_b32_e32 v49, 5, v10
	v_lshl_add_u64 v[4:5], s[14:15], 0, v[4:5]
	s_lshl_b32 s52, s23, 7
	v_lshl_add_u64 v[4:5], v[4:5], 0, s[52:53]
	v_lshlrev_b32_e32 v0, 4, v49
	v_lshl_add_u64 v[12:13], v[4:5], 0, v[0:1]
	s_mov_b32 s5, 0x5c00000
	v_add_co_u32_e32 v4, vcc, s5, v12
	s_mov_b32 s5, 0x5c08000
	s_nop 0
	v_addc_co_u32_e32 v5, vcc, 0, v13, vcc
	s_mov_b64 s[26:27], 0x5c00000
	v_add_co_u32_e32 v36, vcc, s5, v12
	v_lshl_add_u64 v[32:33], v[12:13], 0, s[26:27]
	s_nop 0
	v_addc_co_u32_e32 v37, vcc, 0, v13, vcc
	s_waitcnt lgkmcnt(0)
	s_barrier

	s_nop 0


	s_nop 0

	s_nop 0

	s_lshl_b32 s4, s4, 13
	v_lshlrev_b32_e32 v2, 4, v10
	s_add_i32 s4, s4, 0
	v_add_u32_e32 v177, s4, v2
	v_lshlrev_b32_e32 v2, 2, v10
	v_ashrrev_i32_e32 v42, 3, v8
	v_ashrrev_i32_e32 v43, 31, v42
	v_and_b32_e32 v54, 7, v8
	v_lshlrev_b32_e32 v46, 4, v54
	v_mov_b32_e32 v47, v1
	v_or_b32_e32 v227, 32, v172
	v_lshlrev_b64 v[50:51], 10, v[42:43]
	v_lshlrev_b32_e32 v55, 2, v49
	s_waitcnt vmcnt(7)
	ds_write_b128 v177, v[60:63] offset:49152
	s_waitcnt vmcnt(6)
	ds_write_b128 v177, v[64:67] offset:53248
	s_waitcnt vmcnt(5)
	ds_write_b128 v177, v[68:71] offset:50176
	s_waitcnt vmcnt(4)
	ds_write_b128 v177, v[72:75] offset:54272
	s_waitcnt vmcnt(3)
	ds_write_b128 v177, v[76:79] offset:51200
	s_waitcnt vmcnt(2)
	ds_write_b128 v177, v[80:83] offset:55296
	s_waitcnt vmcnt(1)
	ds_write_b128 v177, v[84:87] offset:52224
	s_waitcnt vmcnt(0)
	ds_write_b128 v177, v[88:91] offset:56320
	global_load_dword v4, v2, s[20:21]
	v_add_u32_e32 v7, 64, v9
	global_load_dword v2, v2, s[8:9]
	v_xor_b32_e32 v9, 1, v234
	v_cmp_lt_i32_e32 vcc, v9, v7
	s_lshl_b32 s20, s25, 3
	s_add_i32 s20, s20, 8
	v_cndmask_b32_e32 v9, v234, v9, vcc
	v_lshlrev_b32_e32 v9, 2, v9
	s_mov_b64 s[8:9], -1
	v_readfirstlane_b32 s21, v0
	s_waitcnt vmcnt(1)
	v_and_b32_e32 v5, 0x7fffffff, v4
	ds_bpermute_b32 v5, v9, v5
	s_waitcnt vmcnt(0)
	v_and_b32_e32 v6, 0x7fffffff, v2
	v_max_f32_e64 v4, |v4|, |v4|
	v_max_f32_e64 v2, |v2|, |v2|
	s_waitcnt lgkmcnt(0)
	v_max_f32_e32 v5, v5, v5
	v_max_f32_e32 v4, v4, v5
	ds_bpermute_b32 v5, v9, v6
	s_waitcnt lgkmcnt(0)
	v_max_f32_e32 v5, v5, v5
	v_max_f32_e32 v2, v2, v5
	v_xor_b32_e32 v5, 2, v234
	v_cmp_lt_i32_e32 vcc, v5, v7
	s_nop 1
	v_cndmask_b32_e32 v5, v234, v5, vcc
	v_lshlrev_b32_e32 v5, 2, v5
	ds_bpermute_b32 v6, v5, v4
	ds_bpermute_b32 v5, v5, v2
	s_waitcnt lgkmcnt(1)
	v_max_f32_e32 v6, v6, v6
	s_waitcnt lgkmcnt(0)
	v_max_f32_e32 v5, v5, v5
	v_max_f32_e32 v2, v2, v5
	v_xor_b32_e32 v5, 4, v234
	v_cmp_lt_i32_e32 vcc, v5, v7
	v_max_f32_e32 v4, v4, v6
	s_nop 0
	v_cndmask_b32_e32 v5, v234, v5, vcc
	v_lshlrev_b32_e32 v5, 2, v5
	ds_bpermute_b32 v6, v5, v4
	ds_bpermute_b32 v5, v5, v2
	s_waitcnt lgkmcnt(1)
	v_max_f32_e32 v6, v6, v6
	s_waitcnt lgkmcnt(0)
	v_max_f32_e32 v5, v5, v5
	v_max_f32_e32 v2, v2, v5
	v_xor_b32_e32 v5, 8, v234
	v_cmp_lt_i32_e32 vcc, v5, v7
	v_max_f32_e32 v4, v4, v6
	s_nop 0
	v_cndmask_b32_e32 v5, v234, v5, vcc
	v_lshlrev_b32_e32 v5, 2, v5
	ds_bpermute_b32 v6, v5, v4
	ds_bpermute_b32 v5, v5, v2
	s_waitcnt lgkmcnt(1)
	v_max_f32_e32 v6, v6, v6
	s_waitcnt lgkmcnt(0)
	v_max_f32_e32 v5, v5, v5
	v_max_f32_e32 v2, v2, v5
	v_xor_b32_e32 v5, 16, v234
	v_cmp_lt_i32_e32 vcc, v5, v7
	v_max_f32_e32 v4, v4, v6
	s_nop 0
	v_cndmask_b32_e32 v5, v234, v5, vcc
	v_lshlrev_b32_e32 v5, 2, v5
	ds_bpermute_b32 v6, v5, v4
	ds_bpermute_b32 v5, v5, v2
	s_waitcnt lgkmcnt(1)
	v_max_f32_e32 v6, v6, v6
	s_waitcnt lgkmcnt(0)
	v_max_f32_e32 v5, v5, v5
	v_max_f32_e32 v2, v2, v5
	v_xor_b32_e32 v5, 32, v234
	v_cmp_lt_i32_e32 vcc, v5, v7
	v_max_f32_e32 v4, v4, v6
	s_nop 0
	v_cndmask_b32_e32 v5, v234, v5, vcc
	v_lshlrev_b32_e32 v226, 2, v5
	ds_bpermute_b32 v5, v226, v4
	s_waitcnt lgkmcnt(0)
	v_max_f32_e32 v5, v5, v5
	v_max_f32_e32 v4, v4, v5
	ds_bpermute_b32 v5, v226, v2
	v_mul_f32_e32 v4, 0x413c5bb7, v4
	s_waitcnt lgkmcnt(0)
	v_max_f32_e32 v5, v5, v5
	v_max_f32_e32 v2, v2, v5
	v_mul_f32_e32 v48, v2, v4
	v_lshl_add_u64 v[4:5], s[16:17], 0, v[42:43]
	v_lshlrev_b64 v[4:5], 10, v[4:5]
	v_lshl_add_u64 v[4:5], s[14:15], 0, v[4:5]
	v_readfirstlane_b32 s4, v48
	v_lshl_add_u64 v[4:5], v[4:5], 0, s[52:53]
	s_cmp_gt_u32 s4, 0x421fffff
	v_lshl_add_u64 v[4:5], v[4:5], 0, v[46:47]
	s_mov_b64 s[4:5], 0x7c00000
	v_lshl_add_u64 v[40:41], v[4:5], 0, s[4:5]
	v_lshlrev_b32_e32 v2, 4, v8
	s_movk_i32 s4, 0x90
	v_mul_lo_u32 v43, v42, s4
	v_mul_u32_u24_e32 v47, 0x90, v3
	v_and_b32_e32 v38, 0x70, v2
	s_cbranch_scc0 .LBB0_420
	global_load_dwordx4 v[34:37], v[40:41], off
	v_mul_lo_u32 v228, v42, s4
	v_lshlrev_b32_e32 v230, 4, v49
	s_add_i32 s4, 0, 0x9000
	v_add_u32_e32 v56, s4, v230
	s_lshl_b64 s[4:5], s[18:19], 21
	v_lshl_add_u64 v[44:45], s[4:5], 0, v[50:51]
	v_or3_b32 v44, v44, s52, v38
	v_mul_u32_u24_e32 v231, 0x90, v3
	v_lshl_add_u64 v[2:3], s[14:15], 0, v[44:45]
	s_mov_b64 s[4:5], 0x7c10000
	v_lshlrev_b32_e32 v229, 4, v54
	s_or_b32 s11, s24, 63
	s_or_b32 s21, s24, 31
	v_lshlrev_b32_e32 v176, 2, v49
	v_mov_b32_e32 v39, v1
	v_lshl_add_u64 v[52:53], v[2:3], 0, s[4:5]
	s_add_i32 s4, s10, 0x200
	v_mov_b32_e32 v58, 0xf149f2ca
	s_mov_b32 s5, 0
	s_mov_b32 s8, 1
	v_mov_b32_e32 v57, 0xf149f2ca
	s_branch .LBB0_410
